# k_gcn gather software-pipelined: double row buffer, next rows issued before accumulating current rows
# speedup vs baseline: 1.0162x; 1.0025x over previous
.LBB2_9:
	v_lshl_or_b32 v34, v36, 8, v54
	buffer_load_dwordx4 v[34:37], v34, s[24:27], 0 offen
	v_lshl_or_b32 v38, v38, 8, v54
	buffer_load_dwordx4 v[38:41], v38, s[24:27], 0 offen
	v_lshl_or_b32 v42, v42, 8, v54
	buffer_load_dwordx4 v[42:45], v42, s[24:27], 0 offen
	v_lshl_or_b32 v46, v46, 8, v54
	buffer_load_dwordx4 v[46:49], v46, s[24:27], 0 offen
	v_add_lshl_u32 v68, v50, s33, 2
	v_subrev_u32_e32 v69, s33, v53
	global_load_dword v64, v68, s[22:23]
	global_load_dword v55, v68, s[22:23] offset:4
	global_load_dword v66, v68, s[22:23] offset:8
	global_load_dword v65, v68, s[22:23] offset:12
.Lkg_A:
	s_waitcnt vmcnt(0)
	s_cmp_ge_i32 s33, s31
	s_cbranch_scc1 .Lkg_finA
	v_cmp_lt_i32_e64 s[34:35], 0, v69
	v_cmp_lt_i32_e64 s[36:37], 1, v69
	v_cmp_lt_i32_e64 s[38:39], 2, v69
	v_cmp_lt_i32_e64 s[40:41], 3, v69
	v_cndmask_b32_e64 v72, v70, v64, s[34:35]
	v_cndmask_b32_e64 v76, v70, v55, s[36:37]
	v_cndmask_b32_e64 v86, v70, v66, s[38:39]
	v_cndmask_b32_e64 v90, v70, v65, s[40:41]
	v_lshl_or_b32 v72, v72, 8, v54
	buffer_load_dwordx4 v[72:75], v72, s[24:27], 0 offen
	v_lshl_or_b32 v76, v76, 8, v54
	buffer_load_dwordx4 v[76:79], v76, s[24:27], 0 offen
	v_lshl_or_b32 v86, v86, 8, v54
	buffer_load_dwordx4 v[86:89], v86, s[24:27], 0 offen
	v_lshl_or_b32 v90, v90, 8, v54
	buffer_load_dwordx4 v[90:93], v90, s[24:27], 0 offen
	s_add_i32 s33, s33, 4
	v_add_lshl_u32 v68, v50, s33, 2
	v_subrev_u32_e32 v69, s33, v53
	global_load_dword v64, v68, s[22:23]
	global_load_dword v55, v68, s[22:23] offset:4
	global_load_dword v66, v68, s[22:23] offset:8
	global_load_dword v65, v68, s[22:23] offset:12
	v_fma_mix_f32 v62, v34, 1.0, v62 op_sel_hi:[1,0,0]
	v_fma_mix_f32 v63, v34, 1.0, v63 op_sel:[1,0,0] op_sel_hi:[1,0,0]
	v_fma_mix_f32 v60, v35, 1.0, v60 op_sel_hi:[1,0,0]
	v_fma_mix_f32 v61, v35, 1.0, v61 op_sel:[1,0,0] op_sel_hi:[1,0,0]
	v_fma_mix_f32 v58, v36, 1.0, v58 op_sel_hi:[1,0,0]
	v_fma_mix_f32 v59, v36, 1.0, v59 op_sel:[1,0,0] op_sel_hi:[1,0,0]
	v_fma_mix_f32 v56, v37, 1.0, v56 op_sel_hi:[1,0,0]
	v_fma_mix_f32 v57, v37, 1.0, v57 op_sel:[1,0,0] op_sel_hi:[1,0,0]
	v_fma_mix_f32 v62, v38, 1.0, v62 op_sel_hi:[1,0,0]
	v_fma_mix_f32 v63, v38, 1.0, v63 op_sel:[1,0,0] op_sel_hi:[1,0,0]
	v_fma_mix_f32 v60, v39, 1.0, v60 op_sel_hi:[1,0,0]
	v_fma_mix_f32 v61, v39, 1.0, v61 op_sel:[1,0,0] op_sel_hi:[1,0,0]
	v_fma_mix_f32 v58, v40, 1.0, v58 op_sel_hi:[1,0,0]
	v_fma_mix_f32 v59, v40, 1.0, v59 op_sel:[1,0,0] op_sel_hi:[1,0,0]
	v_fma_mix_f32 v56, v41, 1.0, v56 op_sel_hi:[1,0,0]
	v_fma_mix_f32 v57, v41, 1.0, v57 op_sel:[1,0,0] op_sel_hi:[1,0,0]
	v_fma_mix_f32 v62, v42, 1.0, v62 op_sel_hi:[1,0,0]
	v_fma_mix_f32 v63, v42, 1.0, v63 op_sel:[1,0,0] op_sel_hi:[1,0,0]
	v_fma_mix_f32 v60, v43, 1.0, v60 op_sel_hi:[1,0,0]
	v_fma_mix_f32 v61, v43, 1.0, v61 op_sel:[1,0,0] op_sel_hi:[1,0,0]
	v_fma_mix_f32 v58, v44, 1.0, v58 op_sel_hi:[1,0,0]
	v_fma_mix_f32 v59, v44, 1.0, v59 op_sel:[1,0,0] op_sel_hi:[1,0,0]
	v_fma_mix_f32 v56, v45, 1.0, v56 op_sel_hi:[1,0,0]
	v_fma_mix_f32 v57, v45, 1.0, v57 op_sel:[1,0,0] op_sel_hi:[1,0,0]
	v_fma_mix_f32 v62, v46, 1.0, v62 op_sel_hi:[1,0,0]
	v_fma_mix_f32 v63, v46, 1.0, v63 op_sel:[1,0,0] op_sel_hi:[1,0,0]
	v_fma_mix_f32 v60, v47, 1.0, v60 op_sel_hi:[1,0,0]
	v_fma_mix_f32 v61, v47, 1.0, v61 op_sel:[1,0,0] op_sel_hi:[1,0,0]
	v_fma_mix_f32 v58, v48, 1.0, v58 op_sel_hi:[1,0,0]
	v_fma_mix_f32 v59, v48, 1.0, v59 op_sel:[1,0,0] op_sel_hi:[1,0,0]
	v_fma_mix_f32 v56, v49, 1.0, v56 op_sel_hi:[1,0,0]
	v_fma_mix_f32 v57, v49, 1.0, v57 op_sel:[1,0,0] op_sel_hi:[1,0,0]
.Lkg_B:
	s_waitcnt vmcnt(0)
	s_cmp_ge_i32 s33, s31
	s_cbranch_scc1 .Lkg_finB
	v_cmp_lt_i32_e64 s[34:35], 0, v69
	v_cmp_lt_i32_e64 s[36:37], 1, v69
	v_cmp_lt_i32_e64 s[38:39], 2, v69
	v_cmp_lt_i32_e64 s[40:41], 3, v69
	v_cndmask_b32_e64 v34, v70, v64, s[34:35]
	v_cndmask_b32_e64 v38, v70, v55, s[36:37]
	v_cndmask_b32_e64 v42, v70, v66, s[38:39]
	v_cndmask_b32_e64 v46, v70, v65, s[40:41]
	v_lshl_or_b32 v34, v34, 8, v54
	buffer_load_dwordx4 v[34:37], v34, s[24:27], 0 offen
	v_lshl_or_b32 v38, v38, 8, v54
	buffer_load_dwordx4 v[38:41], v38, s[24:27], 0 offen
	v_lshl_or_b32 v42, v42, 8, v54
	buffer_load_dwordx4 v[42:45], v42, s[24:27], 0 offen
	v_lshl_or_b32 v46, v46, 8, v54
	buffer_load_dwordx4 v[46:49], v46, s[24:27], 0 offen
	s_add_i32 s33, s33, 4
	v_add_lshl_u32 v68, v50, s33, 2
	v_subrev_u32_e32 v69, s33, v53
	global_load_dword v64, v68, s[22:23]
	global_load_dword v55, v68, s[22:23] offset:4
	global_load_dword v66, v68, s[22:23] offset:8
	global_load_dword v65, v68, s[22:23] offset:12
	v_fma_mix_f32 v62, v72, 1.0, v62 op_sel_hi:[1,0,0]
	v_fma_mix_f32 v63, v72, 1.0, v63 op_sel:[1,0,0] op_sel_hi:[1,0,0]
	v_fma_mix_f32 v60, v73, 1.0, v60 op_sel_hi:[1,0,0]
	v_fma_mix_f32 v61, v73, 1.0, v61 op_sel:[1,0,0] op_sel_hi:[1,0,0]
	v_fma_mix_f32 v58, v74, 1.0, v58 op_sel_hi:[1,0,0]
	v_fma_mix_f32 v59, v74, 1.0, v59 op_sel:[1,0,0] op_sel_hi:[1,0,0]
	v_fma_mix_f32 v56, v75, 1.0, v56 op_sel_hi:[1,0,0]
	v_fma_mix_f32 v57, v75, 1.0, v57 op_sel:[1,0,0] op_sel_hi:[1,0,0]
	v_fma_mix_f32 v62, v76, 1.0, v62 op_sel_hi:[1,0,0]
	v_fma_mix_f32 v63, v76, 1.0, v63 op_sel:[1,0,0] op_sel_hi:[1,0,0]
	v_fma_mix_f32 v60, v77, 1.0, v60 op_sel_hi:[1,0,0]
	v_fma_mix_f32 v61, v77, 1.0, v61 op_sel:[1,0,0] op_sel_hi:[1,0,0]
	v_fma_mix_f32 v58, v78, 1.0, v58 op_sel_hi:[1,0,0]
	v_fma_mix_f32 v59, v78, 1.0, v59 op_sel:[1,0,0] op_sel_hi:[1,0,0]
	v_fma_mix_f32 v56, v79, 1.0, v56 op_sel_hi:[1,0,0]
	v_fma_mix_f32 v57, v79, 1.0, v57 op_sel:[1,0,0] op_sel_hi:[1,0,0]
	v_fma_mix_f32 v62, v86, 1.0, v62 op_sel_hi:[1,0,0]
	v_fma_mix_f32 v63, v86, 1.0, v63 op_sel:[1,0,0] op_sel_hi:[1,0,0]
	v_fma_mix_f32 v60, v87, 1.0, v60 op_sel_hi:[1,0,0]
	v_fma_mix_f32 v61, v87, 1.0, v61 op_sel:[1,0,0] op_sel_hi:[1,0,0]
	v_fma_mix_f32 v58, v88, 1.0, v58 op_sel_hi:[1,0,0]
	v_fma_mix_f32 v59, v88, 1.0, v59 op_sel:[1,0,0] op_sel_hi:[1,0,0]
	v_fma_mix_f32 v56, v89, 1.0, v56 op_sel_hi:[1,0,0]
	v_fma_mix_f32 v57, v89, 1.0, v57 op_sel:[1,0,0] op_sel_hi:[1,0,0]
	v_fma_mix_f32 v62, v90, 1.0, v62 op_sel_hi:[1,0,0]
	v_fma_mix_f32 v63, v90, 1.0, v63 op_sel:[1,0,0] op_sel_hi:[1,0,0]
	v_fma_mix_f32 v60, v91, 1.0, v60 op_sel_hi:[1,0,0]
	v_fma_mix_f32 v61, v91, 1.0, v61 op_sel:[1,0,0] op_sel_hi:[1,0,0]
	v_fma_mix_f32 v58, v92, 1.0, v58 op_sel_hi:[1,0,0]
	v_fma_mix_f32 v59, v92, 1.0, v59 op_sel:[1,0,0] op_sel_hi:[1,0,0]
	v_fma_mix_f32 v56, v93, 1.0, v56 op_sel_hi:[1,0,0]
	v_fma_mix_f32 v57, v93, 1.0, v57 op_sel:[1,0,0] op_sel_hi:[1,0,0]
	s_branch .Lkg_A
.Lkg_finA:
	v_fma_mix_f32 v62, v34, 1.0, v62 op_sel_hi:[1,0,0]
	v_fma_mix_f32 v63, v34, 1.0, v63 op_sel:[1,0,0] op_sel_hi:[1,0,0]
	v_fma_mix_f32 v60, v35, 1.0, v60 op_sel_hi:[1,0,0]
	v_fma_mix_f32 v61, v35, 1.0, v61 op_sel:[1,0,0] op_sel_hi:[1,0,0]
	v_fma_mix_f32 v58, v36, 1.0, v58 op_sel_hi:[1,0,0]
	v_fma_mix_f32 v59, v36, 1.0, v59 op_sel:[1,0,0] op_sel_hi:[1,0,0]
	v_fma_mix_f32 v56, v37, 1.0, v56 op_sel_hi:[1,0,0]
	v_fma_mix_f32 v57, v37, 1.0, v57 op_sel:[1,0,0] op_sel_hi:[1,0,0]
	v_fma_mix_f32 v62, v38, 1.0, v62 op_sel_hi:[1,0,0]
	v_fma_mix_f32 v63, v38, 1.0, v63 op_sel:[1,0,0] op_sel_hi:[1,0,0]
	v_fma_mix_f32 v60, v39, 1.0, v60 op_sel_hi:[1,0,0]
	v_fma_mix_f32 v61, v39, 1.0, v61 op_sel:[1,0,0] op_sel_hi:[1,0,0]
	v_fma_mix_f32 v58, v40, 1.0, v58 op_sel_hi:[1,0,0]
	v_fma_mix_f32 v59, v40, 1.0, v59 op_sel:[1,0,0] op_sel_hi:[1,0,0]
	v_fma_mix_f32 v56, v41, 1.0, v56 op_sel_hi:[1,0,0]
	v_fma_mix_f32 v57, v41, 1.0, v57 op_sel:[1,0,0] op_sel_hi:[1,0,0]
	v_fma_mix_f32 v62, v42, 1.0, v62 op_sel_hi:[1,0,0]
	v_fma_mix_f32 v63, v42, 1.0, v63 op_sel:[1,0,0] op_sel_hi:[1,0,0]
	v_fma_mix_f32 v60, v43, 1.0, v60 op_sel_hi:[1,0,0]
	v_fma_mix_f32 v61, v43, 1.0, v61 op_sel:[1,0,0] op_sel_hi:[1,0,0]
	v_fma_mix_f32 v58, v44, 1.0, v58 op_sel_hi:[1,0,0]
	v_fma_mix_f32 v59, v44, 1.0, v59 op_sel:[1,0,0] op_sel_hi:[1,0,0]
	v_fma_mix_f32 v56, v45, 1.0, v56 op_sel_hi:[1,0,0]
	v_fma_mix_f32 v57, v45, 1.0, v57 op_sel:[1,0,0] op_sel_hi:[1,0,0]
	v_fma_mix_f32 v62, v46, 1.0, v62 op_sel_hi:[1,0,0]
	v_fma_mix_f32 v63, v46, 1.0, v63 op_sel:[1,0,0] op_sel_hi:[1,0,0]
	v_fma_mix_f32 v60, v47, 1.0, v60 op_sel_hi:[1,0,0]
	v_fma_mix_f32 v61, v47, 1.0, v61 op_sel:[1,0,0] op_sel_hi:[1,0,0]
	v_fma_mix_f32 v58, v48, 1.0, v58 op_sel_hi:[1,0,0]
	v_fma_mix_f32 v59, v48, 1.0, v59 op_sel:[1,0,0] op_sel_hi:[1,0,0]
	v_fma_mix_f32 v56, v49, 1.0, v56 op_sel_hi:[1,0,0]
	v_fma_mix_f32 v57, v49, 1.0, v57 op_sel:[1,0,0] op_sel_hi:[1,0,0]
	s_branch .LBB2_19
.Lkg_finB:
	v_fma_mix_f32 v62, v72, 1.0, v62 op_sel_hi:[1,0,0]
	v_fma_mix_f32 v63, v72, 1.0, v63 op_sel:[1,0,0] op_sel_hi:[1,0,0]
	v_fma_mix_f32 v60, v73, 1.0, v60 op_sel_hi:[1,0,0]
	v_fma_mix_f32 v61, v73, 1.0, v61 op_sel:[1,0,0] op_sel_hi:[1,0,0]
	v_fma_mix_f32 v58, v74, 1.0, v58 op_sel_hi:[1,0,0]
	v_fma_mix_f32 v59, v74, 1.0, v59 op_sel:[1,0,0] op_sel_hi:[1,0,0]
	v_fma_mix_f32 v56, v75, 1.0, v56 op_sel_hi:[1,0,0]
	v_fma_mix_f32 v57, v75, 1.0, v57 op_sel:[1,0,0] op_sel_hi:[1,0,0]
	v_fma_mix_f32 v62, v76, 1.0, v62 op_sel_hi:[1,0,0]
	v_fma_mix_f32 v63, v76, 1.0, v63 op_sel:[1,0,0] op_sel_hi:[1,0,0]
	v_fma_mix_f32 v60, v77, 1.0, v60 op_sel_hi:[1,0,0]
	v_fma_mix_f32 v61, v77, 1.0, v61 op_sel:[1,0,0] op_sel_hi:[1,0,0]
	v_fma_mix_f32 v58, v78, 1.0, v58 op_sel_hi:[1,0,0]
	v_fma_mix_f32 v59, v78, 1.0, v59 op_sel:[1,0,0] op_sel_hi:[1,0,0]
	v_fma_mix_f32 v56, v79, 1.0, v56 op_sel_hi:[1,0,0]
	v_fma_mix_f32 v57, v79, 1.0, v57 op_sel:[1,0,0] op_sel_hi:[1,0,0]
	v_fma_mix_f32 v62, v86, 1.0, v62 op_sel_hi:[1,0,0]
	v_fma_mix_f32 v63, v86, 1.0, v63 op_sel:[1,0,0] op_sel_hi:[1,0,0]
	v_fma_mix_f32 v60, v87, 1.0, v60 op_sel_hi:[1,0,0]
	v_fma_mix_f32 v61, v87, 1.0, v61 op_sel:[1,0,0] op_sel_hi:[1,0,0]
	v_fma_mix_f32 v58, v88, 1.0, v58 op_sel_hi:[1,0,0]
	v_fma_mix_f32 v59, v88, 1.0, v59 op_sel:[1,0,0] op_sel_hi:[1,0,0]
	v_fma_mix_f32 v56, v89, 1.0, v56 op_sel_hi:[1,0,0]
	v_fma_mix_f32 v57, v89, 1.0, v57 op_sel:[1,0,0] op_sel_hi:[1,0,0]
	v_fma_mix_f32 v62, v90, 1.0, v62 op_sel_hi:[1,0,0]
	v_fma_mix_f32 v63, v90, 1.0, v63 op_sel:[1,0,0] op_sel_hi:[1,0,0]
	v_fma_mix_f32 v60, v91, 1.0, v60 op_sel_hi:[1,0,0]
	v_fma_mix_f32 v61, v91, 1.0, v61 op_sel:[1,0,0] op_sel_hi:[1,0,0]
	v_fma_mix_f32 v58, v92, 1.0, v58 op_sel_hi:[1,0,0]
	v_fma_mix_f32 v59, v92, 1.0, v59 op_sel:[1,0,0] op_sel_hi:[1,0,0]
	v_fma_mix_f32 v56, v93, 1.0, v56 op_sel_hi:[1,0,0]
	v_fma_mix_f32 v57, v93, 1.0, v57 op_sel:[1,0,0] op_sel_hi:[1,0,0]
